# MoE unit loops: expert lookup of a unit as one per-lane LDS read + compare + popcount instead of the 6-step dependent binary search
# speedup vs baseline: 1.0125x; 1.0020x over previous
.LBB0_1007:
	s_ashr_i32 s10, s46, 31
	s_lshr_b32 s10, s10, 29
	s_add_i32 s10, s46, s10
	s_ashr_i32 s36, s10, 3
	s_mov_b64 s[98:99], exec
	s_mov_b64 exec, -1
	v_and_b32_e32 v2, 63, v250
	v_lshlrev_b32_e32 v2, 2, v2
	v_add_u32_e32 v2, 0x20000, v2
	ds_read_b32 v2, v2
	s_waitcnt lgkmcnt(0)
	v_cmp_ge_i32_e64 s[100:101], s36, v2
	s_bcnt1_i32_b64 s10, s[100:101]
	s_add_i32 s10, s10, -1
	s_mov_b64 exec, s[98:99]
	s_lshl_b32 s34, s10, 2
	s_add_i32 s34, s34, 0
	s_add_i32 s34, s34, 0x20000
	v_mov_b32_e32 v2, s34
	ds_read2_b32 v[4:5], v2 offset1:80
	ds_read_b32 v2, v2 offset:640
	s_mul_i32 s34, s10, 0x44
	s_add_i32 s48, s34, 0
	s_lshl_b32 s47, s10, 13
	s_waitcnt lgkmcnt(1)
	v_readfirstlane_b32 s35, v4
	s_sub_i32 s35, s36, s35
	v_readfirstlane_b32 s37, v5
	s_lshl_b32 s49, s35, 9
	s_sub_i32 s35, s37, s49
	s_min_i32 s50, s35, 0x200
	s_add_i32 s48, s48, 0x20400
	v_cmp_gt_i32_e32 vcc, s50, v0
	v_mov_b32_e32 v136, 0
	v_mov_b32_e32 v3, 0
	s_and_saveexec_b64 s[34:35], vcc
	s_cbranch_execz .LBB0_1011
	v_mov_b32_e32 v3, s48
	ds_read_b32 v3, v3 offset:32
	v_add_u32_e32 v4, s49, v0
	s_waitcnt lgkmcnt(0)
	v_cmp_gt_i32_e32 vcc, v3, v4
	s_nop 1
	v_cndmask_b32_e64 v3, 8, 0, vcc
	v_lshl_add_u32 v5, v3, 2, s48
	ds_read_b32 v5, v5 offset:16
	v_or_b32_e32 v6, 4, v3
	s_waitcnt lgkmcnt(0)
	v_cmp_gt_i32_e32 vcc, v5, v4
	s_nop 1
	v_cndmask_b32_e32 v3, v6, v3, vcc
	v_lshl_add_u32 v5, v3, 2, s48
	ds_read_b32 v5, v5 offset:8
	v_or_b32_e32 v6, 2, v3
	s_waitcnt lgkmcnt(0)
	v_cmp_gt_i32_e32 vcc, v5, v4
	s_nop 1
	v_cndmask_b32_e32 v3, v6, v3, vcc
	v_lshl_add_u32 v5, v3, 2, s48
	ds_read_b32 v5, v5 offset:4
	v_or_b32_e32 v6, 1, v3
	s_waitcnt lgkmcnt(0)
	v_cmp_gt_i32_e32 vcc, v5, v4
	s_nop 1
	v_cndmask_b32_e32 v3, v6, v3, vcc
	v_lshl_add_u32 v5, v3, 2, s48
	ds_read_b32 v5, v5
	v_add_u32_e32 v4, s47, v4
	s_waitcnt lgkmcnt(0)
	v_sub_u32_e32 v4, v4, v5
	v_lshl_add_u32 v4, v3, 9, v4
	v_ashrrev_i32_e32 v5, 31, v4
	v_lshl_add_u64 v[4:5], v[4:5], 2, s[6:7]
	global_load_dword v3, v[4:5], off
	s_waitcnt vmcnt(0)
	v_lshlrev_b32_e32 v3, 11, v3
	v_and_b32_e32 v3, 0x7fff800, v3

.LBB0_1083:
	s_ashr_i32 s10, s46, 31
	s_lshr_b32 s10, s10, 28
	s_add_i32 s10, s46, s10
	s_ashr_i32 s10, s10, 4
	s_mov_b64 s[98:99], exec
	s_mov_b64 exec, -1
	v_and_b32_e32 v2, 63, v250
	v_lshlrev_b32_e32 v2, 2, v2
	v_add_u32_e32 v2, 0x20000, v2
	ds_read_b32 v2, v2
	s_waitcnt lgkmcnt(0)
	v_cmp_ge_i32_e64 s[100:101], s10, v2
	s_bcnt1_i32_b64 s34, s[100:101]
	s_add_i32 s34, s34, -1
	s_mov_b64 exec, s[98:99]
	s_lshl_b32 s30, s34, 2
	s_add_i32 s30, s30, 0
	s_add_i32 s30, s30, 0x20000
	v_mov_b32_e32 v4, s30
	ds_read2_b32 v[2:3], v4 offset1:80
	ds_read_b32 v4, v4 offset:640
	s_mov_b32 s35, s11
	s_waitcnt lgkmcnt(1)
	v_readfirstlane_b32 s30, v2
	s_sub_i32 s30, s10, s30
	v_readfirstlane_b32 s31, v3
	s_lshl_b32 s47, s30, 9
	s_waitcnt lgkmcnt(0)
	v_readfirstlane_b32 s49, v4
	s_sub_i32 s30, s31, s47
	s_add_i32 s49, s49, s47
	s_min_i32 s48, s30, 0x200
	s_lshl_b64 s[30:31], s[34:35], 22
	s_add_u32 s35, s6, s30
	s_addc_u32 s50, s7, s31
	s_lshl_b32 s10, s10, 11
	s_lshl_b32 s30, s46, 7
	s_sub_i32 s30, s30, s10
	s_ashr_i32 s31, s30, 31
	v_cmp_gt_i32_e32 vcc, s48, v0
	s_lshl_b64 s[36:37], s[30:31], 2
	s_add_u32 s36, s35, s36
	v_cndmask_b32_e32 v2, 0, v0, vcc
	v_add_u32_e32 v2, s49, v2
	s_addc_u32 s37, s50, s37
	v_lshl_or_b32 v146, v2, 9, v1
	v_lshl_add_u64 v[2:3], s[36:37], 0, v[152:153]
	v_lshl_add_u64 v[154:155], v[2:3], 0, v[148:149]
	s_mov_b64 s[36:37], -1
	s_cmp_ge_i32 s38, s48
	v_lshl_add_u64 v[132:133], v[154:155], 0, s[20:21]
	v_lshl_add_u64 v[130:131], v[154:155], 0, s[22:23]
	v_lshl_add_u64 v[134:135], v[154:155], 0, s[24:25]
	v_lshl_add_u64 v[138:139], v[154:155], 0, s[26:27]
	v_lshl_add_u64 v[142:143], v[154:155], 0, s[28:29]
	s_cbranch_scc0 .LBB0_1089
	global_load_dwordx4 v[2:5], v[154:155], off sc1 nt
	s_mov_b32 m0, s39
	global_load_dwordx4 v[6:9], v[132:133], off sc1 nt
	v_lshl_add_u64 v[82:83], s[12:13], 0, v[146:147]
	global_load_lds_dwordx4 v146, s[12:13]
	global_load_dwordx4 v[66:69], v[130:131], off sc1 nt
	global_load_dwordx4 v[70:73], v[134:135], off sc1 nt
	s_mov_b32 m0, s40
	s_nop 0
	global_load_lds_dwordx4 v146, s[14:15]
	s_waitcnt vmcnt(4)
	s_nop 0
	v_cvt_pk_bf16_f32 v2, v2, v6
	ds_write_b32 v167, v2 offset:49152
	v_cvt_pk_bf16_f32 v2, v3, v7
	ds_write_b32 v167, v2 offset:49216
	v_cvt_pk_bf16_f32 v2, v4, v8
	ds_write_b32 v167, v2 offset:49280
	v_cvt_pk_bf16_f32 v2, v5, v9
	ds_write_b32 v167, v2 offset:49344
	global_load_dwordx4 v[74:77], v[138:139], off sc1 nt
	global_load_dwordx4 v[78:81], v[142:143], off sc1 nt
	s_waitcnt vmcnt(5)
	s_mov_b32 m0, s41
	s_waitcnt lgkmcnt(0)
	s_barrier
	global_load_lds_dwordx4 v146, s[16:17]
	v_mov_b32_e32 v2, 0
	s_mov_b32 s36, -2
	s_movk_i32 s35, 0x80
	v_mov_b32_e32 v3, v2
	v_mov_b32_e32 v4, v2
	v_mov_b32_e32 v5, v2
	v_mov_b32_e32 v6, v2
	v_mov_b32_e32 v7, v2
	v_mov_b32_e32 v8, v2
	v_mov_b32_e32 v9, v2
	v_mov_b32_e32 v10, v2
	v_mov_b32_e32 v11, v2
	v_mov_b32_e32 v12, v2
	v_mov_b32_e32 v13, v2
	v_mov_b32_e32 v14, v2
	v_mov_b32_e32 v15, v2
	v_mov_b32_e32 v16, v2
	v_mov_b32_e32 v17, v2
	v_mov_b32_e32 v18, v2
	v_mov_b32_e32 v19, v2
	v_mov_b32_e32 v20, v2
	v_mov_b32_e32 v21, v2
	v_mov_b32_e32 v22, v2
	v_mov_b32_e32 v23, v2
	v_mov_b32_e32 v24, v2
	v_mov_b32_e32 v25, v2
	v_mov_b32_e32 v26, v2
	v_mov_b32_e32 v27, v2
	v_mov_b32_e32 v28, v2
	v_mov_b32_e32 v29, v2
	v_mov_b32_e32 v30, v2
	v_mov_b32_e32 v31, v2
	v_mov_b32_e32 v32, v2
	v_mov_b32_e32 v33, v2
	v_mov_b32_e32 v34, v2
	v_mov_b32_e32 v35, v2
	v_mov_b32_e32 v36, v2
	v_mov_b32_e32 v37, v2
	v_mov_b32_e32 v38, v2
	v_mov_b32_e32 v39, v2
	v_mov_b32_e32 v40, v2
	v_mov_b32_e32 v41, v2
	v_mov_b32_e32 v42, v2
	v_mov_b32_e32 v43, v2
	v_mov_b32_e32 v44, v2
	v_mov_b32_e32 v45, v2
	v_mov_b32_e32 v46, v2
	v_mov_b32_e32 v47, v2
	v_mov_b32_e32 v48, v2
	v_mov_b32_e32 v49, v2
	v_mov_b32_e32 v50, v2
	v_mov_b32_e32 v51, v2
	v_mov_b32_e32 v52, v2
	v_mov_b32_e32 v53, v2
	v_mov_b32_e32 v54, v2
	v_mov_b32_e32 v55, v2
	v_mov_b32_e32 v56, v2
	v_mov_b32_e32 v57, v2
	v_mov_b32_e32 v58, v2
	v_mov_b32_e32 v59, v2
	v_mov_b32_e32 v60, v2
	v_mov_b32_e32 v61, v2
	v_mov_b32_e32 v62, v2
	v_mov_b32_e32 v63, v2
	v_mov_b32_e32 v64, v2
	v_mov_b32_e32 v65, v2
	v_readfirstlane_b32 s98, v250
	s_bitcmp1_b32 s98, 6
	s_cbranch_scc1 .Lmoe_B_1087
